# best version plus prep-kernel kernarg scalar loads merged up front (prologue de-serialisation)
# speedup vs baseline: 1.0110x; 1.0110x over previous
_Z11prep_kernelPKfPDF16_Pf:
	s_load_dwordx4 s[4:7], s[0:1], 0x0
	s_load_dwordx2 s[8:9], s[0:1], 0x10
	v_lshrrev_b32_e32 v1, 6, v0
	v_lshl_or_b32 v8, s2, 2, v1
	v_ashrrev_i32_e32 v9, 31, v8
	v_and_b32_e32 v18, 63, v0
	v_lshlrev_b64 v[2:3], 10, v[8:9]
	s_waitcnt lgkmcnt(0)
	v_lshl_add_u64 v[2:3], s[4:5], 0, v[2:3]
	v_lshlrev_b32_e32 v6, 4, v18
	v_mov_b32_e32 v7, 0
	v_lshl_add_u64 v[2:3], v[2:3], 0, v[6:7]
	global_load_dwordx4 v[2:5], v[2:3], off
	v_mbcnt_lo_u32_b32 v1, -1, 0
	v_mbcnt_hi_u32_b32 v1, -1, v1
	v_and_b32_e32 v6, 64, v1
	v_xor_b32_e32 v10, 32, v1
	v_add_u32_e32 v6, 64, v6
	v_cmp_lt_i32_e32 vcc, v10, v6
	s_waitcnt vmcnt(0)
	v_cvt_f64_f32_e32 v[12:13], v3
	v_cndmask_b32_e32 v10, v1, v10, vcc
	v_lshlrev_b32_e32 v19, 2, v10
	v_cvt_f64_f32_e32 v[10:11], v2
	v_mul_f64 v[12:13], v[12:13], v[12:13]
	v_cvt_f64_f32_e32 v[14:15], v4
	v_fmac_f64_e32 v[12:13], v[10:11], v[10:11]
	v_cvt_f64_f32_e32 v[16:17], v5
	v_fmac_f64_e32 v[12:13], v[14:15], v[14:15]
	v_fmac_f64_e32 v[12:13], v[16:17], v[16:17]
	ds_bpermute_b32 v10, v19, v12
	ds_bpermute_b32 v11, v19, v13
	v_xor_b32_e32 v14, 16, v1
	v_cmp_lt_i32_e32 vcc, v14, v6
	s_waitcnt lgkmcnt(0)
	v_add_f64 v[10:11], v[12:13], v[10:11]
	v_cndmask_b32_e32 v14, v1, v14, vcc
	v_lshlrev_b32_e32 v14, 2, v14
	ds_bpermute_b32 v12, v14, v10
	ds_bpermute_b32 v13, v14, v11
	v_xor_b32_e32 v14, 8, v1
	v_cmp_lt_i32_e32 vcc, v14, v6
	s_waitcnt lgkmcnt(0)
	v_add_f64 v[10:11], v[10:11], v[12:13]
	v_cndmask_b32_e32 v14, v1, v14, vcc
	v_lshlrev_b32_e32 v14, 2, v14
	ds_bpermute_b32 v12, v14, v10
	ds_bpermute_b32 v13, v14, v11
	v_xor_b32_e32 v14, 4, v1
	v_cmp_lt_i32_e32 vcc, v14, v6
	s_waitcnt lgkmcnt(0)
	v_add_f64 v[10:11], v[10:11], v[12:13]
	v_cndmask_b32_e32 v14, v1, v14, vcc
	v_lshlrev_b32_e32 v14, 2, v14
	ds_bpermute_b32 v12, v14, v10
	ds_bpermute_b32 v13, v14, v11
	v_xor_b32_e32 v14, 2, v1
	v_cmp_lt_i32_e32 vcc, v14, v6
	s_waitcnt lgkmcnt(0)
	v_add_f64 v[10:11], v[10:11], v[12:13]
	v_cndmask_b32_e32 v14, v1, v14, vcc
	v_lshlrev_b32_e32 v14, 2, v14
	ds_bpermute_b32 v12, v14, v10
	ds_bpermute_b32 v13, v14, v11
	v_xor_b32_e32 v14, 1, v1
	v_cmp_lt_i32_e32 vcc, v14, v6
	s_waitcnt lgkmcnt(0)
	v_add_f64 v[10:11], v[10:11], v[12:13]
	v_cndmask_b32_e32 v1, v1, v14, vcc
	v_lshlrev_b32_e32 v1, 2, v1
	ds_bpermute_b32 v12, v1, v10
	ds_bpermute_b32 v13, v1, v11
	v_lshlrev_b32_e32 v1, 2, v18
	v_cmp_eq_u32_e32 vcc, 0, v18
	s_and_saveexec_b64 s[2:3], vcc
	s_cbranch_execz .LBB0_2
	s_waitcnt lgkmcnt(0)
	v_add_f64 v[10:11], v[10:11], v[12:13]
	v_mul_f64 v[10:11], v[10:11], 0.5
	v_cvt_f32_f64_e32 v6, v[10:11]
	v_lshl_add_u64 v[12:13], v[8:9], 2, s[8:9]
	global_store_dword v[12:13], v6, off

	.amdhsa_kernel _Z11prep_kernelPKfPDF16_Pf
		.amdhsa_group_segment_fixed_size 0
		.amdhsa_private_segment_fixed_size 0
		.amdhsa_kernarg_size 24
		.amdhsa_user_sgpr_count 2
		.amdhsa_user_sgpr_dispatch_ptr 0
		.amdhsa_user_sgpr_queue_ptr 0
		.amdhsa_user_sgpr_kernarg_segment_ptr 1
		.amdhsa_user_sgpr_dispatch_id 0
		.amdhsa_user_sgpr_kernarg_preload_length 0
		.amdhsa_user_sgpr_kernarg_preload_offset 0
		.amdhsa_user_sgpr_private_segment_size 0
		.amdhsa_uses_dynamic_stack 0
		.amdhsa_enable_private_segment 0
		.amdhsa_system_sgpr_workgroup_id_x 1
		.amdhsa_system_sgpr_workgroup_id_y 0
		.amdhsa_system_sgpr_workgroup_id_z 0
		.amdhsa_system_sgpr_workgroup_info 0
		.amdhsa_system_vgpr_workitem_id 0
		.amdhsa_next_free_vgpr 20
		.amdhsa_next_free_sgpr 10
		.amdhsa_accum_offset 20
		.amdhsa_reserve_vcc 1
		.amdhsa_float_round_mode_32 0
		.amdhsa_float_round_mode_16_64 0
		.amdhsa_float_denorm_mode_32 3
		.amdhsa_float_denorm_mode_16_64 3
		.amdhsa_dx10_clamp 1
		.amdhsa_ieee_mode 1
		.amdhsa_fp16_overflow 0
		.amdhsa_tg_split 0
		.amdhsa_exception_fp_ieee_invalid_op 0
		.amdhsa_exception_fp_denorm_src 0
		.amdhsa_exception_fp_ieee_div_zero 0
		.amdhsa_exception_fp_ieee_overflow 0
		.amdhsa_exception_fp_ieee_underflow 0
		.amdhsa_exception_fp_ieee_inexact 0
		.amdhsa_exception_int_div_zero 0
	.end_amdhsa_kernel

amdhsa.kernels:
  - .agpr_count:     0
    .args:
      - .actual_access:  read_only
        .address_space:  global
        .offset:         0
        .size:           8
        .value_kind:     global_buffer
      - .actual_access:  write_only
        .address_space:  global
        .offset:         8
        .size:           8
        .value_kind:     global_buffer
      - .actual_access:  write_only
        .address_space:  global
        .offset:         16
        .size:           8
        .value_kind:     global_buffer
    .group_segment_fixed_size: 0
    .kernarg_segment_align: 8
    .kernarg_segment_size: 24
    .language:       OpenCL C
    .language_version:
      - 2
      - 0
    .max_flat_workgroup_size: 256
    .name:           _Z11prep_kernelPKfPDF16_Pf
    .private_segment_fixed_size: 0
    .sgpr_count:     16
    .sgpr_spill_count: 0
    .symbol:         _Z11prep_kernelPKfPDF16_Pf.kd
    .uniform_work_group_size: 1
    .uses_dynamic_stack: false
    .vgpr_count:     20
    .vgpr_spill_count: 0
    .wavefront_size: 64
  - .agpr_count:     0
    .args:
      - .address_space:  global
        .offset:         0
        .size:           8
        .value_kind:     global_buffer
      - .address_space:  global
        .offset:         8
        .size:           8
        .value_kind:     global_buffer
      - .actual_access:  read_only
        .address_space:  global
        .offset:         16
        .size:           8
        .value_kind:     global_buffer
      - .actual_access:  read_only
        .address_space:  global
        .offset:         24
        .size:           8
        .value_kind:     global_buffer
      - .address_space:  global
        .offset:         32
        .size:           8
        .value_kind:     global_buffer
      - .address_space:  global
        .offset:         40
        .size:           8
        .value_kind:     global_buffer
    .group_segment_fixed_size: 142400
    .kernarg_segment_align: 8
    .kernarg_segment_size: 48
    .language:       OpenCL C
    .language_version:
      - 2
      - 0
    .max_flat_workgroup_size: 512
    .name:           _Z11main_kernelPKfS0_PKDF16_S0_PfS3_
    .private_segment_fixed_size: 0
    .sgpr_count:     108
    .sgpr_spill_count: 1
    .symbol:         _Z11main_kernelPKfS0_PKDF16_S0_PfS3_.kd
    .uniform_work_group_size: 1
    .uses_dynamic_stack: false
    .vgpr_count:     217
    .vgpr_spill_count: 0
    .wavefront_size: 64
